# baseline (speedup 1.0000x reference)
.Lg1_cloop:
	s_lshl_b32 s12, s8, 14
	v_add3_u32 v42, s12, v37, v35
	v_add3_u32 v58, s12, v36, v35
	s_waitcnt vmcnt(3)
	s_barrier
	s_lshl_b32 s13, s17, 14
	s_add_i32 m0, s13, s16
	s_add_i32 s13, s17, 1
	global_load_lds_dwordx4 v62, s[14:15]
	s_cmp_lg_u32 s17, 4
	s_cselect_b32 s17, s13, 0
	v_add_u32_e32 v62, 64, v62
	ds_read_b128 v[38:41], v42 offset:8192
	ds_read_b128 v[42:45], v42 offset:9216
	ds_read_b128 v[46:49], v58
	ds_read_b128 v[50:53], v58 offset:1024
	ds_read_b128 v[54:57], v58 offset:2048
	ds_read_b128 v[58:61], v58 offset:3072
	s_waitcnt lgkmcnt(0)
	v_mfma_f32_16x16x32_f16 v[30:33], v[46:49], v[38:41], v[30:33]
	s_add_i32 s12, s8, 1
	s_cmp_lg_u32 s8, 4
	s_cselect_b32 s8, s12, 0
	v_mfma_f32_16x16x32_f16 v[22:25], v[46:49], v[42:45], v[22:25]
	s_add_i32 s11, s11, -1
	s_cmp_eq_u32 s11, 0
	v_mfma_f32_16x16x32_f16 v[26:29], v[50:53], v[38:41], v[26:29]
	v_mfma_f32_16x16x32_f16 v[14:17], v[50:53], v[42:45], v[14:17]
	v_mfma_f32_16x16x32_f16 v[18:21], v[54:57], v[38:41], v[18:21]
	v_mfma_f32_16x16x32_f16 v[6:9], v[54:57], v[42:45], v[6:9]
	v_mfma_f32_16x16x32_f16 v[10:13], v[58:61], v[38:41], v[10:13]
	v_mfma_f32_16x16x32_f16 v[2:5], v[58:61], v[42:45], v[2:5]
	s_cbranch_scc0 .Lg1_cloop
	s_or_b32 s8, s10, s4
	v_or_b32_e32 v35, s8, v34
	v_lshl_or_b32 v34, v1, 2, s9
	v_mov_b32_e32 v37, 0
	v_or_b32_e32 v34, s7, v34
	v_lshlrev_b32_e32 v36, 12, v35
	v_mov_b32_e32 v35, v37
	v_lshl_add_u64 v[38:39], s[2:3], 0, v[36:37]
	v_lshlrev_b64 v[40:41], 2, v[34:35]
	v_lshl_add_u64 v[42:43], v[38:39], 0, v[40:41]
	s_mov_b64 s[2:3], 0x10000
	v_lshl_add_u64 v[44:45], v[42:43], 0, s[2:3]
	global_store_dwordx4 v[42:43], v[30:33], off sc1
	global_store_dwordx4 v[42:43], v[26:29], off offset:64 sc1
	global_store_dwordx4 v[42:43], v[18:21], off offset:128 sc1
	global_store_dwordx4 v[42:43], v[10:13], off offset:192 sc1
	global_store_dwordx4 v[44:45], v[22:25], off sc1
	global_store_dwordx4 v[44:45], v[14:17], off offset:64 sc1
	global_store_dwordx4 v[44:45], v[6:9], off offset:128 sc1
	global_store_dwordx4 v[44:45], v[2:5], off offset:192 sc1
	s_branch .LBB3_2
